# v039 + diff MFMA segment regenerated (no prefetch before barrier): rows-0..31 chain first, persistent seed tuple, spread splat, next addresses at M end
# baseline (speedup 1.0000x reference)
; #define PK4(P, BASE, OUT) do { u32x4 w = {cvtpk(P[BASE + 0], P[BASE + 1]), cvtpk(P[BASE + 2], P[BASE + 3]), cvtpk(P[BASE + 4], P[BASE + 5]), cvtpk(P[BASE + 6], P[BASE + 7])}; \
;     OUT = *reinterpret_cast<bf16x8*>(&w); } while (0)
; __device__ __forceinline__ void smax_tile(f32x16& p0, f32x16& p1, float& mhat, float& l_reg, f32x16 (&o)[4], float* al_l, const bool first, int r32, int hi,
;                                           bf16x8& pa0, bf16x8& pa1, bf16x8& pa2, bf16x8& pa3) {
;     ...
; #pragma unroll
;     for (int r = 0; r < 16; ++r) p0[r] = __builtin_amdgcn_exp2f(p0[r]);
; #pragma unroll
;     for (int r = 0; r < 16; ++r) p1[r] = __builtin_amdgcn_exp2f(p1[r]);
;     float ps = p0[0];
; #pragma unroll
;     for (int r = 1; r < 16; ++r) ps += p0[r];
; #pragma unroll
;     for (int r = 0; r < 16; ++r) ps += p1[r];
;     { auto rr = __builtin_amdgcn_permlane32_swap(__float_as_uint(ps), __float_as_uint(ps), false, false); ps = __uint_as_float(rr[0]) + __uint_as_float(rr[1]); }
;     l_reg += ps;
;     ...
;     PK4(p0, 0, pa0); PK4(p0, 8, pa1); PK4(p1, 0, pa2); PK4(p1, 8, pa3);
.LBB0_651:
	v_exp_f32_e32 v96, v96
	v_exp_f32_e32 v97, v97
	v_exp_f32_e32 v98, v98
	v_exp_f32_e32 v99, v99
	v_exp_f32_e32 v100, v100
	v_exp_f32_e32 v101, v101
	v_add_f32_e32 v128, v96, v97
	v_exp_f32_e32 v102, v102
	v_add_f32_e32 v128, v98, v128
	v_exp_f32_e32 v103, v103
	v_add_f32_e32 v128, v99, v128
	v_exp_f32_e32 v104, v104
	v_add_f32_e32 v128, v100, v128
	v_exp_f32_e32 v105, v105
	v_add_f32_e32 v128, v101, v128
	v_exp_f32_e32 v106, v106
	v_add_f32_e32 v128, v102, v128
	v_exp_f32_e32 v107, v107
	v_add_f32_e32 v128, v103, v128
	v_exp_f32_e32 v108, v108
	v_add_f32_e32 v128, v104, v128
	v_exp_f32_e32 v109, v109
	v_add_f32_e32 v128, v105, v128
	v_exp_f32_e32 v110, v110
	v_add_f32_e32 v128, v106, v128
	v_exp_f32_e32 v111, v111
	v_add_f32_e32 v128, v107, v128
	v_exp_f32_e32 v80, v80
	v_add_f32_e32 v128, v108, v128
	v_exp_f32_e32 v81, v81
	v_add_f32_e32 v128, v109, v128
	v_exp_f32_e32 v82, v82
	v_add_f32_e32 v128, v110, v128
	v_exp_f32_e32 v83, v83
	v_add_f32_e32 v128, v111, v128
	v_exp_f32_e32 v84, v84
	v_add_f32_e32 v128, v80, v128
	v_exp_f32_e32 v85, v85
	v_add_f32_e32 v128, v81, v128
	v_exp_f32_e32 v86, v86
	v_add_f32_e32 v128, v82, v128
	v_exp_f32_e32 v87, v87
	v_add_f32_e32 v128, v83, v128
	v_exp_f32_e32 v88, v88
	v_add_f32_e32 v128, v84, v128
	v_exp_f32_e32 v89, v89
	v_add_f32_e32 v128, v85, v128
	v_exp_f32_e32 v90, v90
	v_add_f32_e32 v128, v86, v128
	v_exp_f32_e32 v91, v91
	v_add_f32_e32 v128, v87, v128
	v_exp_f32_e32 v92, v92
	v_add_f32_e32 v128, v88, v128
	v_exp_f32_e32 v93, v93
	v_add_f32_e32 v128, v89, v128
	v_exp_f32_e32 v94, v94
	v_add_f32_e32 v128, v90, v128
	v_exp_f32_e32 v95, v95
	v_add_f32_e32 v128, v91, v128
	v_add_f32_e32 v128, v92, v128
	v_add_f32_e32 v128, v93, v128
	v_add_f32_e32 v128, v94, v128
	v_add_f32_e32 v128, v95, v128
	v_mov_b32_e32 v129, v128
	v_cvt_pk_bf16_f32 v162, v96, v97
	v_cvt_pk_bf16_f32 v163, v98, v99
	v_permlane32_swap_b32_e32 v128, v129
	v_add_f32_e32 v128, v128, v129
	v_add_f32_e32 v159, v159, v128
	v_cvt_pk_bf16_f32 v164, v100, v101
	v_cvt_pk_bf16_f32 v165, v102, v103
	v_cvt_pk_bf16_f32 v166, v104, v105
	v_cvt_pk_bf16_f32 v167, v106, v107
	v_cvt_pk_bf16_f32 v168, v108, v109
	v_cvt_pk_bf16_f32 v169, v110, v111
	v_cvt_pk_bf16_f32 v132, v80, v81
	v_cvt_pk_bf16_f32 v133, v82, v83
	v_cvt_pk_bf16_f32 v134, v84, v85
	v_cvt_pk_bf16_f32 v135, v86, v87
	v_cvt_pk_bf16_f32 v128, v88, v89
	v_cvt_pk_bf16_f32 v129, v90, v91
	v_cvt_pk_bf16_f32 v130, v92, v93
	v_cvt_pk_bf16_f32 v131, v94, v95
	s_waitcnt lgkmcnt(0)
	s_barrier
; #define SBAR() __builtin_amdgcn_sched_barrier(0)
; #define LWN1(a) do { if constexpr (NW == 0) LW1(0, a); else if constexpr (NW == 1) LW1(1, a); else if constexpr (NW == 2) LW1(2, a); else if constexpr (NW == 3) LW1(3, a); else if constexpr (NW == 4) LW1(4, a); else if constexpr (NW == 5) LW1(5, a); else LW1(6, a); } while (0)
; #define LWN2(a, b) do { if constexpr (NW == 0) LW2(0, a, b); else if constexpr (NW == 1) LW2(1, a, b); else if constexpr (NW == 2) LW2(2, a, b); else if constexpr (NW == 3) LW2(3, a, b); else if constexpr (NW == 4) LW2(4, a, b); else if constexpr (NW == 5) LW2(5, a, b); else LW2(6, a, b); } while (0)
; template <int DQK, bool HASQK, bool HASPV, int J> ...
;     constexpr int NQS = HASQK ? 2 * (DQK / 16) : 0, NS = NQS + (HASPV ? 16 : 0);
;     if constexpr (J < NS) {
;         constexpr int rd1 = (J + 1 < NS) ? ((J + 1 < NQS) ? 1 : 2) : 0, rd2 = (J + 2 < NS) ? ((J + 2 < NQS) ? 1 : 2) : 0, rd3 = (J + 3 < NS) ? ((J + 3 < NQS) ? 1 : 2) : 0, NW = rd1 + rd2 + rd3;
;     ...
;         if constexpr (J < NQS) { constexpr int d0 = J >> 1, h = J & 1;
;             LWN1(kf[d0][h]); SBAR();
;             if constexpr (h == 0) p0 = __builtin_amdgcn_mfma_f32_32x32x16_bf16(kf[d0][0], qr[d0], (d0 == 0) ? negm : p0, 0, 0, 0);
;             else p1 = __builtin_amdgcn_mfma_f32_32x32x16_bf16(kf[d0][1], qr[d0], (d0 == 0) ? negm : p1, 0, 0, 0);
;         } else { constexpr int q = J - NQS, g = q >> 2, d = q & 3;
;             LWN2(vf[g][2 * d], vf[g][2 * d + 1]); SBAR();
;             o[d] = __builtin_amdgcn_mfma_f32_32x32x16_bf16(pa[g], (bf16x8){vf[g][2 * d][0], vf[g][2 * d][1], vf[g][2 * d][2], vf[g][2 * d][3], vf[g][2 * d + 1][0], vf[g][2 * d + 1][1], vf[g][2 * d + 1][2], vf[g][2 * d + 1][3]}, o[d], 0, 0, 0);
;         }
;     ...
;         SBAR();
;         slot_read<DQK, HASQK, HASPV, J + 4>(kf, vf, ka_, vb_);
;         SBAR();
;         slot_run<DQK, HASQK, HASPV, J + 1>(kf, vf, ka_, vb_, qr, p0, p1, negm, o, pa);
	ds_read_b128 v[170:173], v232 offset:0
	ds_read_b128 v[174:177], v233 offset:0
	ds_read_b128 v[178:181], v186 offset:0
	ds_read_b128 v[182:185], v187 offset:0
	s_waitcnt lgkmcnt(3)
	v_mfma_f32_32x32x16_bf16 v[96:111], v[170:173], v[112:115], v[200:215]
	v_xor_b32_e32 v80, 0x80000000, v158
	v_mov_b32_e32 v81, v80
	v_mov_b32_e32 v82, v80
	v_mov_b32_e32 v83, v80
	v_mov_b32_e32 v84, v80
	ds_read_b128 v[170:173], v232 offset:4096
	s_waitcnt lgkmcnt(3)
	v_mfma_f32_32x32x16_bf16 v[96:111], v[174:177], v[116:119], v[96:111]
	v_mov_b32_e32 v85, v80
	v_mov_b32_e32 v86, v80
	v_mov_b32_e32 v87, v80
	v_mov_b32_e32 v88, v80
	ds_read_b128 v[174:177], v233 offset:4096
	s_waitcnt lgkmcnt(3)
	v_mfma_f32_32x32x16_bf16 v[96:111], v[178:181], v[120:123], v[96:111]
	v_mov_b32_e32 v89, v80
	v_mov_b32_e32 v90, v80
	v_mov_b32_e32 v91, v80
	v_mov_b32_e32 v92, v80
	ds_read_b128 v[178:181], v186 offset:4096
	s_waitcnt lgkmcnt(3)
	v_mfma_f32_32x32x16_bf16 v[96:111], v[182:185], v[124:127], v[96:111]
	v_mov_b32_e32 v93, v80
	v_mov_b32_e32 v94, v80
	v_mov_b32_e32 v95, v80
	ds_read_b128 v[182:185], v187 offset:4096
	s_waitcnt lgkmcnt(3)
	v_mfma_f32_32x32x16_bf16 v[80:95], v[170:173], v[112:115], v[80:95]
	ds_read_b64_tr_b16 v[170:171], v188 offset:0
	ds_read_b64_tr_b16 v[172:173], v188 offset:2048
	s_waitcnt lgkmcnt(4)
	v_mfma_f32_32x32x16_bf16 v[80:95], v[174:177], v[116:119], v[80:95]
	ds_read_b64_tr_b16 v[174:175], v188 offset:512
	ds_read_b64_tr_b16 v[176:177], v188 offset:2560
	s_waitcnt lgkmcnt(5)
	v_mfma_f32_32x32x16_bf16 v[80:95], v[178:181], v[120:123], v[80:95]
	ds_read_b64_tr_b16 v[178:179], v188 offset:1024
	ds_read_b64_tr_b16 v[180:181], v188 offset:3072
	s_waitcnt lgkmcnt(6)
	v_mfma_f32_32x32x16_bf16 v[80:95], v[182:185], v[124:127], v[80:95]
	ds_read_b64_tr_b16 v[182:183], v188 offset:1536
	ds_read_b64_tr_b16 v[184:185], v188 offset:3584
	s_waitcnt lgkmcnt(6)
	v_mfma_f32_32x32x16_bf16 v[64:79], v[162:165], v[170:173], v[64:79]
	ds_read_b64_tr_b16 v[170:171], v188 offset:4096
	ds_read_b64_tr_b16 v[172:173], v188 offset:6144
	s_waitcnt lgkmcnt(6)
	v_mfma_f32_32x32x16_bf16 v[48:63], v[162:165], v[174:177], v[48:63]
	ds_read_b64_tr_b16 v[174:175], v188 offset:4608
	ds_read_b64_tr_b16 v[176:177], v188 offset:6656
	s_waitcnt lgkmcnt(6)
	v_mfma_f32_32x32x16_bf16 v[32:47], v[162:165], v[178:181], v[32:47]
	ds_read_b64_tr_b16 v[178:179], v188 offset:5120
	ds_read_b64_tr_b16 v[180:181], v188 offset:7168
	s_waitcnt lgkmcnt(6)
	v_mfma_f32_32x32x16_bf16 v[16:31], v[162:165], v[182:185], v[16:31]
	ds_read_b64_tr_b16 v[182:183], v188 offset:5632
	ds_read_b64_tr_b16 v[184:185], v188 offset:7680
	s_waitcnt lgkmcnt(6)
	v_mfma_f32_32x32x16_bf16 v[64:79], v[166:169], v[170:173], v[64:79]
	ds_read_b64_tr_b16 v[170:171], v188 offset:8192
	ds_read_b64_tr_b16 v[172:173], v188 offset:10240
	s_waitcnt lgkmcnt(6)
	v_mfma_f32_32x32x16_bf16 v[48:63], v[166:169], v[174:177], v[48:63]
	ds_read_b64_tr_b16 v[174:175], v188 offset:8704
	ds_read_b64_tr_b16 v[176:177], v188 offset:10752
	s_waitcnt lgkmcnt(6)
	v_mfma_f32_32x32x16_bf16 v[32:47], v[166:169], v[178:181], v[32:47]
	ds_read_b64_tr_b16 v[178:179], v188 offset:9216
	ds_read_b64_tr_b16 v[180:181], v188 offset:11264
	s_waitcnt lgkmcnt(6)
	v_mfma_f32_32x32x16_bf16 v[16:31], v[166:169], v[182:185], v[16:31]
	ds_read_b64_tr_b16 v[182:183], v188 offset:9728
	ds_read_b64_tr_b16 v[184:185], v188 offset:11776
	s_waitcnt lgkmcnt(6)
	v_mfma_f32_32x32x16_bf16 v[64:79], v[132:135], v[170:173], v[64:79]
	ds_read_b64_tr_b16 v[170:171], v188 offset:12288
	ds_read_b64_tr_b16 v[172:173], v188 offset:14336
	s_waitcnt lgkmcnt(6)
	v_mfma_f32_32x32x16_bf16 v[48:63], v[132:135], v[174:177], v[48:63]
	ds_read_b64_tr_b16 v[174:175], v188 offset:12800
	ds_read_b64_tr_b16 v[176:177], v188 offset:14848
	s_waitcnt lgkmcnt(6)
	v_mfma_f32_32x32x16_bf16 v[32:47], v[132:135], v[178:181], v[32:47]
	ds_read_b64_tr_b16 v[178:179], v188 offset:13312
	ds_read_b64_tr_b16 v[180:181], v188 offset:15360
	s_waitcnt lgkmcnt(6)
	v_mfma_f32_32x32x16_bf16 v[16:31], v[132:135], v[182:185], v[16:31]
	ds_read_b64_tr_b16 v[182:183], v188 offset:13824
	ds_read_b64_tr_b16 v[184:185], v188 offset:15872
	s_waitcnt lgkmcnt(6)
	v_mfma_f32_32x32x16_bf16 v[64:79], v[128:131], v[170:173], v[64:79]
	s_waitcnt lgkmcnt(4)
	v_mfma_f32_32x32x16_bf16 v[48:63], v[128:131], v[174:177], v[48:63]
	s_waitcnt lgkmcnt(2)
	v_mfma_f32_32x32x16_bf16 v[32:47], v[128:131], v[178:181], v[32:47]
	s_waitcnt lgkmcnt(0)
	v_mfma_f32_32x32x16_bf16 v[16:31], v[128:131], v[182:185], v[16:31]
	v_lshl_add_u64 v[144:145], v[144:145], 0, s[28:29]
	v_lshl_add_u64 v[146:147], v[146:147], 0, s[28:29]
	v_lshl_add_u64 v[148:149], v[148:149], 0, s[28:29]
	s_add_i32 s46, s86, 1
	s_cmp_lg_u32 s86, 2
	s_cselect_b32 s46, s46, 0
	s_lshl_b32 s47, s46, 13
	s_lshl_b32 s46, s86, 14
	v_add_u32_e32 v188, s46, v157
	v_add_u32_e32 v232, s47, v141
	v_add_u32_e32 v233, s47, v143
	v_add_u32_e32 v186, s47, v160
	v_add_u32_e32 v187, s47, v161
	s_waitcnt vmcnt(0)
	s_add_u32 s44, s44, 0x10000
	s_waitcnt lgkmcnt(0)
	s_barrier
	s_addc_u32 s45, s45, 0
	s_cmp_eq_u32 s44, 0x7f0000
	s_cbranch_scc1 .LBB0_662
